# MLA H=0 step: waves 0-3 run the exp2/pack block before their QK MFMAs, waves 4-7 keep MFMAs first (role asymmetry within a SIMD), on top of the K prefetch
# baseline (speedup 1.0000x reference)
.LBB0_570:
	s_cmp_gt_u32 s81, 0xff
	s_cbranch_scc1 .Lmla_hi_c0
	v_exp_f32_e32 v97, v179
	v_exp_f32_e32 v96, v178
	v_exp_f32_e32 v100, v162
	v_exp_f32_e32 v101, v163
	v_exp_f32_e32 v104, v158
	v_exp_f32_e32 v105, v159
	v_exp_f32_e32 v108, v154
	v_exp_f32_e32 v109, v155
	v_exp_f32_e32 v98, v176
	v_exp_f32_e32 v99, v177
	v_exp_f32_e32 v102, v160
	v_exp_f32_e32 v103, v161
	v_cvt_pk_fp8_f32 v144, v96, v97
	v_cvt_pk_fp8_f32 v145, v100, v101
	v_exp_f32_e32 v106, v156
	v_exp_f32_e32 v107, v157
	v_exp_f32_e32 v110, v152
	v_cvt_pk_fp8_f32 v146, v104, v105
	v_exp_f32_e32 v104, v153
	v_cvt_pk_fp8_f32 v147, v108, v109
	v_cvt_pk_fp8_f32 v144, v98, v99 op_sel:[0,0,1]
	v_cvt_pk_fp8_f32 v145, v102, v103 op_sel:[0,0,1]
	v_cvt_pk_fp8_f32 v146, v106, v107 op_sel:[0,0,1]
	v_cvt_pk_fp8_f32 v147, v110, v104 op_sel:[0,0,1]

.Lmla_back_b0:
	s_cmp_gt_u32 s81, 0xff
	s_cbranch_scc0 .Lmla_lo_b0
	v_exp_f32_e32 v97, v179
	v_exp_f32_e32 v96, v178
	v_exp_f32_e32 v100, v162
	v_exp_f32_e32 v101, v163
	v_exp_f32_e32 v104, v158
	v_exp_f32_e32 v105, v159
	v_exp_f32_e32 v108, v154
	v_exp_f32_e32 v109, v155
	v_exp_f32_e32 v98, v176
	v_exp_f32_e32 v99, v177
	v_exp_f32_e32 v102, v160
	v_exp_f32_e32 v103, v161
	v_cvt_pk_fp8_f32 v144, v96, v97
	v_cvt_pk_fp8_f32 v145, v100, v101
	s_xor_b32 s18, s24, 0x8000
	v_exp_f32_e32 v106, v156
	v_exp_f32_e32 v107, v157
	v_exp_f32_e32 v110, v152
	v_cvt_pk_fp8_f32 v146, v104, v105
	v_exp_f32_e32 v104, v153
	v_cvt_pk_fp8_f32 v147, v108, v109
	v_add_u32_e32 v105, s18, v216
	v_cvt_pk_fp8_f32 v144, v98, v99 op_sel:[0,0,1]
	v_cvt_pk_fp8_f32 v145, v102, v103 op_sel:[0,0,1]
	s_waitcnt lgkmcnt(0)
	s_barrier
	ds_read_b128 v[96:99], v105
	ds_read_b128 v[100:103], v105 offset:16
	ds_read_b128 v[156:159], v105 offset:64
	ds_read_b128 v[160:163], v105 offset:80
	v_add_u32_e32 v105, v105, v217
	ds_read_b128 v[148:151], v105 offset:128
	ds_read_b128 v[152:155], v105 offset:160
	v_cvt_pk_fp8_f32 v146, v106, v107 op_sel:[0,0,1]
	v_cvt_pk_fp8_f32 v147, v110, v104 op_sel:[0,0,1]
.Lmla_join_b0:
	v_cmp_gt_f32_e32 vcc, 1.0, v191
	s_cbranch_vccz .LBB0_565
	s_and_saveexec_b64 s[18:19], s[2:3]
	s_cbranch_execz .LBB0_564
	ds_write_b32 v209, v191 offset:128
	s_branch .LBB0_564

.Lmla_lo_b0:
	s_xor_b32 s18, s24, 0x8000
	v_add_u32_e32 v105, s18, v216
	s_waitcnt lgkmcnt(0)
	s_barrier
	ds_read_b128 v[96:99], v105
	ds_read_b128 v[100:103], v105 offset:16
	ds_read_b128 v[156:159], v105 offset:64
	ds_read_b128 v[160:163], v105 offset:80
	v_add_u32_e32 v105, v105, v217
	ds_read_b128 v[148:151], v105 offset:128
	ds_read_b128 v[152:155], v105 offset:160
	s_branch .Lmla_join_b0

.Lmla_back_b1:
	s_cmp_gt_u32 s81, 0xff
	s_cbranch_scc0 .Lmla_lo_b1
	v_exp_f32_e32 v97, v179
	v_exp_f32_e32 v96, v178
	v_exp_f32_e32 v100, v162
	v_exp_f32_e32 v101, v163
	v_exp_f32_e32 v104, v158
	v_exp_f32_e32 v105, v159
	v_exp_f32_e32 v108, v154
	v_exp_f32_e32 v109, v155
	v_exp_f32_e32 v98, v176
	v_exp_f32_e32 v99, v177
	v_exp_f32_e32 v102, v160
	v_exp_f32_e32 v103, v161
	v_cvt_pk_fp8_f32 v144, v96, v97
	v_cvt_pk_fp8_f32 v145, v100, v101
	s_xor_b32 s20, s25, 0x8000
	v_exp_f32_e32 v106, v156
	v_exp_f32_e32 v107, v157
	v_exp_f32_e32 v110, v152
	v_cvt_pk_fp8_f32 v146, v104, v105
	v_exp_f32_e32 v104, v153
	v_cvt_pk_fp8_f32 v147, v108, v109
	v_add_u32_e32 v105, s20, v214
	v_cvt_pk_fp8_f32 v144, v98, v99 op_sel:[0,0,1]
	v_cvt_pk_fp8_f32 v145, v102, v103 op_sel:[0,0,1]
	s_waitcnt lgkmcnt(0)
	s_barrier
	ds_read_b128 v[96:99], v105
	ds_read_b128 v[100:103], v105 offset:16
	ds_read_b128 v[156:159], v105 offset:64
	ds_read_b128 v[160:163], v105 offset:80
	v_add_u32_e32 v105, v105, v215
	ds_read_b128 v[148:151], v105 offset:128
	ds_read_b128 v[152:155], v105 offset:160
	v_cvt_pk_fp8_f32 v146, v106, v107 op_sel:[0,0,1]
	v_cvt_pk_fp8_f32 v147, v110, v104 op_sel:[0,0,1]
.Lmla_join_b1:
	v_cmp_gt_f32_e32 vcc, 1.0, v193
	s_cbranch_vccz .LBB0_1875
	s_and_saveexec_b64 s[20:21], s[2:3]
	s_cbranch_execz .LBB0_1874
	ds_write_b32 v208, v193 offset:128
	s_branch .LBB0_1874

.Lmla_lo_b1:
	s_xor_b32 s20, s25, 0x8000
	v_add_u32_e32 v105, s20, v214
	s_waitcnt lgkmcnt(0)
	s_barrier
	ds_read_b128 v[96:99], v105
	ds_read_b128 v[100:103], v105 offset:16
	ds_read_b128 v[156:159], v105 offset:64
	ds_read_b128 v[160:163], v105 offset:80
	v_add_u32_e32 v105, v105, v215
	ds_read_b128 v[148:151], v105 offset:128
	ds_read_b128 v[152:155], v105 offset:160
	s_branch .Lmla_join_b1
